# sparse attention stagger: waves 4-7 defer each query's output block (scale, bf16 convert, stores) behind the next query's LDS row staging, waves 0-3 keep it at the end of the query; on top of e1
# baseline (speedup 1.0000x reference)
.LBB0_803:
	s_cmp_lt_u32 s44, 0x100
	s_cbranch_scc1 .Lsp_older
	s_or_b64 exec, exec, s[8:9]
	v_readlane_b32 s8, v253, 22
	s_add_i32 s14, s14, 1
	s_mov_b32 s99, 1
	s_nop 0
	v_lshl_add_u32 v152, v88, 2, s8
	ds_read_b128 v[132:135], v152
	ds_read_b128 v[136:139], v152 offset:32
	ds_read_b128 v[140:143], v152 offset:64
	ds_read_b128 v[144:147], v152 offset:96
	s_andn2_b64 vcc, exec, s[6:7]
	s_mov_b32 s16, s15
	s_nop 0
	s_cbranch_vccz .Lsp_drain
	s_branch .LBB0_804
